# adds: MoE down epilogue scale fold (bias x16 once, 64 pk_mul removed); O2 row-scale epilogues: ssq loads of rows 1..7 hoisted with counted vmcnt
# speedup vs baseline: 1.0157x; 1.0157x over previous
.LBB0_491:
	s_lshl_b32 s0, s0, 8
	v_mov_b32_e32 v1, v0
	s_add_i32 s0, s0, s46
	s_nop 15
	s_nop 7
	s_nop 0
	v_and_or_b32 v142, v1, 15, s0
	v_ashrrev_i32_e32 v143, 31, v142
	v_lshlrev_b64 v[144:145], 6, v[142:143]
	v_lshl_add_u64 v[144:145], s[10:11], 0, v[144:145]
	global_load_dwordx4 v[148:151], v[144:145], off offset:32
	global_load_dwordx4 v[156:159], v[144:145], off offset:1056
	global_load_dwordx4 v[160:163], v[144:145], off offset:2080
	global_load_dwordx4 v[164:167], v[144:145], off offset:3104
	s_mov_b64 vcc, 0x2000
	v_lshl_add_u64 v[184:185], v[144:145], 0, vcc
	global_load_dwordx4 v[168:171], v[184:185], off offset:32
	global_load_dwordx4 v[172:175], v[184:185], off offset:1056
	global_load_dwordx4 v[176:179], v[184:185], off offset:2080
	global_load_dwordx4 v[180:183], v[184:185], off offset:3104
	s_lshl_b32 s0, s1, 8
	v_lshrrev_b32_e32 v1, 1, v1
	v_and_or_b32 v1, v1, 24, s0
	v_or_b32_e32 v140, s47, v1
	v_ashrrev_i32_e32 v141, 31, v140
	s_waitcnt vmcnt(7)
	v_mov_b32_e32 v144, v149
	v_mov_b32_e32 v145, v150
	v_mov_b32_e32 v149, v151
	v_pk_add_f32 v[144:145], v[144:145], v[148:149]
	v_mov_b32_e32 v150, v3
	v_add_f32_e32 v1, v144, v145
	v_add_f32_e32 v1, 0, v1
	v_fmamk_f32 v1, v1, 0x3b800000, v220
	v_cmp_gt_f32_e32 vcc, s93, v1
	v_mul_f32_e32 v144, 0x4f800000, v1
	v_mov_b32_e32 v151, v3
	v_cndmask_b32_e32 v1, v1, v144, vcc
	v_sqrt_f32_e32 v144, v1
	s_nop 0
	v_add_u32_e32 v145, -1, v144
	v_fma_f32 v147, -v145, v144, v1
	v_cmp_ge_f32_e64 s[0:1], 0, v147
	v_add_u32_e32 v147, 1, v144
	s_nop 0
	v_cndmask_b32_e64 v145, v144, v145, s[0:1]
	v_fma_f32 v144, -v147, v144, v1
	v_cmp_lt_f32_e64 s[0:1], 0, v144
	s_nop 1
	v_cndmask_b32_e64 v144, v145, v147, s[0:1]
	v_mul_f32_e32 v145, 0x37800000, v144
	v_cndmask_b32_e32 v144, v144, v145, vcc
	v_cmp_class_f32_e32 vcc, v1, v221
	s_nop 1
	v_cndmask_b32_e32 v1, v144, v1, vcc
	v_div_scale_f32 v144, s[0:1], v1, v1, s74
	v_rcp_f32_e32 v145, v144
	s_nop 0
	v_fma_f32 v147, -v144, v145, 1.0
	v_fmac_f32_e32 v145, v147, v145
	v_div_scale_f32 v147, vcc, s74, v1, s74
	v_mul_f32_e32 v148, v147, v145
	v_fma_f32 v149, -v144, v148, v147
	v_fmac_f32_e32 v148, v149, v145
	v_fma_f32 v144, -v144, v148, v147
	v_div_fmas_f32 v144, v144, v145, v148
	v_div_fixup_f32 v148, v144, v1, s74
	v_pk_mul_f32 v[128:129], v[128:129], v[148:149] op_sel_hi:[1,0]
	v_pk_mul_f32 v[132:133], v[132:133], v[148:149] op_sel_hi:[1,0]
	v_cvt_pk_fp8_f32 v150, v128, v129
	v_pk_mul_f32 v[120:121], v[120:121], v[148:149] op_sel_hi:[1,0]
	v_pk_mul_f32 v[124:125], v[124:125], v[148:149] op_sel_hi:[1,0]
	v_mov_b32_e32 v128, v3
	v_mov_b32_e32 v129, v3
	v_cvt_pk_fp8_f32 v151, v132, v133
	v_cvt_pk_fp8_f32 v128, v120, v121
	v_cvt_pk_fp8_f32 v129, v124, v125
	v_pk_mul_f32 v[130:131], v[130:131], v[148:149] op_sel_hi:[1,0]
	v_pk_mul_f32 v[134:135], v[134:135], v[148:149] op_sel_hi:[1,0]
	v_pk_mul_f32 v[122:123], v[122:123], v[148:149] op_sel_hi:[1,0]
	v_pk_mul_f32 v[126:127], v[126:127], v[148:149] op_sel_hi:[1,0]
	v_cvt_pk_fp8_f32 v150, v130, v131 op_sel:[0,0,1]
	v_cvt_pk_fp8_f32 v151, v134, v135 op_sel:[0,0,1]
	v_cvt_pk_fp8_f32 v128, v122, v123 op_sel:[0,0,1]
	v_cvt_pk_fp8_f32 v129, v126, v127 op_sel:[0,0,1]
	v_lshlrev_b64 v[144:145], 11, v[142:143]
	v_lshl_add_u64 v[144:145], s[8:9], 0, v[144:145]
	v_or_b32_e32 v120, 16, v142
	v_lshl_add_u64 v[144:145], v[144:145], 0, v[140:141]
	v_ashrrev_i32_e32 v121, 31, v120
	global_store_dwordx2 v[144:145], v[150:151], off
	global_store_dwordx2 v[144:145], v[128:129], off offset:128
	v_lshlrev_b64 v[122:123], 6, v[120:121]
	v_lshl_add_u64 v[122:123], s[10:11], 0, v[122:123]
	v_lshlrev_b64 v[120:121], 11, v[120:121]
	v_lshl_add_u64 v[120:121], s[8:9], 0, v[120:121]
	v_lshl_add_u64 v[120:121], v[120:121], 0, v[140:141]
	s_waitcnt vmcnt(8)
	v_mov_b32_e32 v122, v156
	v_mov_b32_e32 v123, v157
	v_mov_b32_e32 v124, v158
	v_mov_b32_e32 v125, v159
	v_mov_b32_e32 v126, v123
	v_mov_b32_e32 v127, v124
	v_mov_b32_e32 v123, v125
	v_pk_add_f32 v[122:123], v[126:127], v[122:123]
	s_nop 0
	v_add_f32_e32 v1, v122, v123
	v_add_f32_e32 v1, 0, v1
	v_fmamk_f32 v1, v1, 0x3b800000, v220
	v_cmp_gt_f32_e32 vcc, s93, v1
	v_mul_f32_e32 v122, 0x4f800000, v1
	s_nop 0
	v_cndmask_b32_e32 v1, v1, v122, vcc
	v_sqrt_f32_e32 v122, v1
	s_nop 0
	v_add_u32_e32 v123, -1, v122
	v_fma_f32 v124, -v123, v122, v1
	v_cmp_ge_f32_e64 s[0:1], 0, v124
	v_add_u32_e32 v124, 1, v122
	s_nop 0
	v_cndmask_b32_e64 v123, v122, v123, s[0:1]
	v_fma_f32 v122, -v124, v122, v1
	v_cmp_lt_f32_e64 s[0:1], 0, v122
	s_nop 1
	v_cndmask_b32_e64 v122, v123, v124, s[0:1]
	v_mul_f32_e32 v123, 0x37800000, v122
	v_cndmask_b32_e32 v122, v122, v123, vcc
	v_cmp_class_f32_e32 vcc, v1, v221
	s_nop 1
	v_cndmask_b32_e32 v1, v122, v1, vcc
	v_div_scale_f32 v122, s[0:1], v1, v1, s74
	v_rcp_f32_e32 v123, v122
	s_nop 0
	v_fma_f32 v124, -v122, v123, 1.0
	v_fmac_f32_e32 v123, v124, v123
	v_div_scale_f32 v124, vcc, s74, v1, s74
	v_mul_f32_e32 v125, v124, v123
	v_fma_f32 v126, -v122, v125, v124
	v_fmac_f32_e32 v125, v126, v123
	v_fma_f32 v122, -v122, v125, v124
	v_div_fmas_f32 v122, v122, v123, v125
	v_div_fixup_f32 v122, v122, v1, s74
	v_pk_mul_f32 v[112:113], v[112:113], v[122:123] op_sel_hi:[1,0]
	v_mov_b32_e32 v124, v3
	v_pk_mul_f32 v[116:117], v[116:117], v[122:123] op_sel_hi:[1,0]
	v_cvt_pk_fp8_f32 v124, v112, v113
	v_mov_b32_e32 v125, v3
	v_pk_mul_f32 v[104:105], v[104:105], v[122:123] op_sel_hi:[1,0]
	v_pk_mul_f32 v[108:109], v[108:109], v[122:123] op_sel_hi:[1,0]
	v_mov_b32_e32 v112, v3
	v_mov_b32_e32 v113, v3
	v_cvt_pk_fp8_f32 v125, v116, v117
	v_cvt_pk_fp8_f32 v112, v104, v105
	v_cvt_pk_fp8_f32 v113, v108, v109
	v_pk_mul_f32 v[114:115], v[114:115], v[122:123] op_sel_hi:[1,0]
	v_pk_mul_f32 v[118:119], v[118:119], v[122:123] op_sel_hi:[1,0]
	v_pk_mul_f32 v[106:107], v[106:107], v[122:123] op_sel_hi:[1,0]
	v_pk_mul_f32 v[110:111], v[110:111], v[122:123] op_sel_hi:[1,0]
	v_cvt_pk_fp8_f32 v124, v114, v115 op_sel:[0,0,1]
	v_cvt_pk_fp8_f32 v125, v118, v119 op_sel:[0,0,1]
	v_cvt_pk_fp8_f32 v112, v106, v107 op_sel:[0,0,1]
	v_cvt_pk_fp8_f32 v113, v110, v111 op_sel:[0,0,1]
	v_or_b32_e32 v104, 32, v142
	v_ashrrev_i32_e32 v105, 31, v104
	global_store_dwordx2 v[120:121], v[124:125], off
	global_store_dwordx2 v[120:121], v[112:113], off offset:128
	v_lshlrev_b64 v[106:107], 6, v[104:105]
	v_lshl_add_u64 v[106:107], s[10:11], 0, v[106:107]
	v_lshlrev_b64 v[104:105], 11, v[104:105]
	v_lshl_add_u64 v[104:105], s[8:9], 0, v[104:105]
	v_lshl_add_u64 v[104:105], v[104:105], 0, v[140:141]
	s_waitcnt vmcnt(9)
	v_mov_b32_e32 v106, v160
	v_mov_b32_e32 v107, v161
	v_mov_b32_e32 v108, v162
	v_mov_b32_e32 v109, v163
	v_mov_b32_e32 v110, v107
	v_mov_b32_e32 v111, v108
	v_mov_b32_e32 v107, v109
	v_pk_add_f32 v[106:107], v[110:111], v[106:107]
	s_nop 0
	v_add_f32_e32 v1, v106, v107
	v_add_f32_e32 v1, 0, v1
	v_fmamk_f32 v1, v1, 0x3b800000, v220
	v_cmp_gt_f32_e32 vcc, s93, v1
	v_mul_f32_e32 v106, 0x4f800000, v1
	s_nop 0
	v_cndmask_b32_e32 v1, v1, v106, vcc
	v_sqrt_f32_e32 v106, v1
	s_nop 0
	v_add_u32_e32 v107, -1, v106
	v_fma_f32 v108, -v107, v106, v1
	v_cmp_ge_f32_e64 s[0:1], 0, v108
	v_add_u32_e32 v108, 1, v106
	s_nop 0
	v_cndmask_b32_e64 v107, v106, v107, s[0:1]
	v_fma_f32 v106, -v108, v106, v1
	v_cmp_lt_f32_e64 s[0:1], 0, v106
	s_nop 1
	v_cndmask_b32_e64 v106, v107, v108, s[0:1]
	v_mul_f32_e32 v107, 0x37800000, v106
	v_cndmask_b32_e32 v106, v106, v107, vcc
	v_cmp_class_f32_e32 vcc, v1, v221
	s_nop 1
	v_cndmask_b32_e32 v1, v106, v1, vcc
	v_div_scale_f32 v106, s[0:1], v1, v1, s74
	v_rcp_f32_e32 v107, v106
	s_nop 0
	v_fma_f32 v108, -v106, v107, 1.0
	v_fmac_f32_e32 v107, v108, v107
	v_div_scale_f32 v108, vcc, s74, v1, s74
	v_mul_f32_e32 v109, v108, v107
	v_fma_f32 v110, -v106, v109, v108
	v_fmac_f32_e32 v109, v110, v107
	v_fma_f32 v106, -v106, v109, v108
	v_div_fmas_f32 v106, v106, v107, v109
	v_div_fixup_f32 v106, v106, v1, s74
	v_pk_mul_f32 v[96:97], v[96:97], v[106:107] op_sel_hi:[1,0]
	v_mov_b32_e32 v108, v3
	v_pk_mul_f32 v[100:101], v[100:101], v[106:107] op_sel_hi:[1,0]
	v_cvt_pk_fp8_f32 v108, v96, v97
	v_mov_b32_e32 v109, v3
	v_pk_mul_f32 v[88:89], v[88:89], v[106:107] op_sel_hi:[1,0]
	v_pk_mul_f32 v[92:93], v[92:93], v[106:107] op_sel_hi:[1,0]
	v_mov_b32_e32 v96, v3
	v_mov_b32_e32 v97, v3
	v_cvt_pk_fp8_f32 v109, v100, v101
	v_cvt_pk_fp8_f32 v96, v88, v89
	v_cvt_pk_fp8_f32 v97, v92, v93
	v_pk_mul_f32 v[98:99], v[98:99], v[106:107] op_sel_hi:[1,0]
	v_pk_mul_f32 v[102:103], v[102:103], v[106:107] op_sel_hi:[1,0]
	v_pk_mul_f32 v[90:91], v[90:91], v[106:107] op_sel_hi:[1,0]
	v_pk_mul_f32 v[94:95], v[94:95], v[106:107] op_sel_hi:[1,0]
	v_cvt_pk_fp8_f32 v108, v98, v99 op_sel:[0,0,1]
	v_cvt_pk_fp8_f32 v109, v102, v103 op_sel:[0,0,1]
	v_cvt_pk_fp8_f32 v96, v90, v91 op_sel:[0,0,1]
	v_cvt_pk_fp8_f32 v97, v94, v95 op_sel:[0,0,1]
	v_or_b32_e32 v88, 48, v142
	v_ashrrev_i32_e32 v89, 31, v88
	global_store_dwordx2 v[104:105], v[108:109], off
	global_store_dwordx2 v[104:105], v[96:97], off offset:128
	v_lshlrev_b64 v[90:91], 6, v[88:89]
	v_lshl_add_u64 v[90:91], s[10:11], 0, v[90:91]
	v_lshlrev_b64 v[88:89], 11, v[88:89]
	v_lshl_add_u64 v[88:89], s[8:9], 0, v[88:89]
	v_lshl_add_u64 v[88:89], v[88:89], 0, v[140:141]
	s_waitcnt vmcnt(10)
	v_mov_b32_e32 v90, v164
	v_mov_b32_e32 v91, v165
	v_mov_b32_e32 v92, v166
	v_mov_b32_e32 v93, v167
	v_mov_b32_e32 v94, v91
	v_mov_b32_e32 v95, v92
	v_mov_b32_e32 v91, v93
	v_pk_add_f32 v[90:91], v[94:95], v[90:91]
	s_nop 0
	v_add_f32_e32 v1, v90, v91
	v_add_f32_e32 v1, 0, v1
	v_fmamk_f32 v1, v1, 0x3b800000, v220
	v_cmp_gt_f32_e32 vcc, s93, v1
	v_mul_f32_e32 v90, 0x4f800000, v1
	s_nop 0
	v_cndmask_b32_e32 v1, v1, v90, vcc
	v_sqrt_f32_e32 v90, v1
	s_nop 0
	v_add_u32_e32 v91, -1, v90
	v_fma_f32 v92, -v91, v90, v1
	v_cmp_ge_f32_e64 s[0:1], 0, v92
	v_add_u32_e32 v92, 1, v90
	s_nop 0
	v_cndmask_b32_e64 v91, v90, v91, s[0:1]
	v_fma_f32 v90, -v92, v90, v1
	v_cmp_lt_f32_e64 s[0:1], 0, v90
	s_nop 1
	v_cndmask_b32_e64 v90, v91, v92, s[0:1]
	v_mul_f32_e32 v91, 0x37800000, v90
	v_cndmask_b32_e32 v90, v90, v91, vcc
	v_cmp_class_f32_e32 vcc, v1, v221
	s_nop 1
	v_cndmask_b32_e32 v1, v90, v1, vcc
	v_div_scale_f32 v90, s[0:1], v1, v1, s74
	v_rcp_f32_e32 v91, v90
	s_nop 0
	v_fma_f32 v92, -v90, v91, 1.0
	v_fmac_f32_e32 v91, v92, v91
	v_div_scale_f32 v92, vcc, s74, v1, s74
	v_mul_f32_e32 v93, v92, v91
	v_fma_f32 v94, -v90, v93, v92
	v_fmac_f32_e32 v93, v94, v91
	v_fma_f32 v90, -v90, v93, v92
	v_div_fmas_f32 v90, v90, v91, v93
	v_div_fixup_f32 v90, v90, v1, s74
	v_pk_mul_f32 v[80:81], v[80:81], v[90:91] op_sel_hi:[1,0]
	v_mov_b32_e32 v92, v3
	v_pk_mul_f32 v[84:85], v[84:85], v[90:91] op_sel_hi:[1,0]
	v_cvt_pk_fp8_f32 v92, v80, v81
	v_mov_b32_e32 v93, v3
	v_pk_mul_f32 v[72:73], v[72:73], v[90:91] op_sel_hi:[1,0]
	v_pk_mul_f32 v[76:77], v[76:77], v[90:91] op_sel_hi:[1,0]
	v_mov_b32_e32 v80, v3
	v_mov_b32_e32 v81, v3
	v_cvt_pk_fp8_f32 v93, v84, v85
	v_cvt_pk_fp8_f32 v80, v72, v73
	v_cvt_pk_fp8_f32 v81, v76, v77
	v_pk_mul_f32 v[82:83], v[82:83], v[90:91] op_sel_hi:[1,0]
	v_pk_mul_f32 v[86:87], v[86:87], v[90:91] op_sel_hi:[1,0]
	v_pk_mul_f32 v[74:75], v[74:75], v[90:91] op_sel_hi:[1,0]
	v_pk_mul_f32 v[78:79], v[78:79], v[90:91] op_sel_hi:[1,0]
	v_cvt_pk_fp8_f32 v92, v82, v83 op_sel:[0,0,1]
	v_cvt_pk_fp8_f32 v93, v86, v87 op_sel:[0,0,1]
	v_cvt_pk_fp8_f32 v80, v74, v75 op_sel:[0,0,1]
	v_cvt_pk_fp8_f32 v81, v78, v79 op_sel:[0,0,1]
	v_add_u32_e32 v72, 0x80, v142
	v_ashrrev_i32_e32 v73, 31, v72
	global_store_dwordx2 v[88:89], v[92:93], off
	global_store_dwordx2 v[88:89], v[80:81], off offset:128
	v_lshlrev_b64 v[74:75], 6, v[72:73]
	v_lshl_add_u64 v[74:75], s[10:11], 0, v[74:75]
	v_lshlrev_b64 v[72:73], 11, v[72:73]
	v_lshl_add_u64 v[72:73], s[8:9], 0, v[72:73]
	v_lshl_add_u64 v[72:73], v[72:73], 0, v[140:141]
	s_waitcnt vmcnt(11)
	v_mov_b32_e32 v74, v168
	v_mov_b32_e32 v75, v169
	v_mov_b32_e32 v76, v170
	v_mov_b32_e32 v77, v171
	v_mov_b32_e32 v78, v75
	v_mov_b32_e32 v79, v76
	v_mov_b32_e32 v75, v77
	v_pk_add_f32 v[74:75], v[78:79], v[74:75]
	s_nop 0
	v_add_f32_e32 v1, v74, v75
	v_add_f32_e32 v1, 0, v1
	v_fmamk_f32 v1, v1, 0x3b800000, v220
	v_cmp_gt_f32_e32 vcc, s93, v1
	v_mul_f32_e32 v74, 0x4f800000, v1
	s_nop 0
	v_cndmask_b32_e32 v1, v1, v74, vcc
	v_sqrt_f32_e32 v74, v1
	s_nop 0
	v_add_u32_e32 v75, -1, v74
	v_fma_f32 v76, -v75, v74, v1
	v_cmp_ge_f32_e64 s[0:1], 0, v76
	v_add_u32_e32 v76, 1, v74
	s_nop 0
	v_cndmask_b32_e64 v75, v74, v75, s[0:1]
	v_fma_f32 v74, -v76, v74, v1
	v_cmp_lt_f32_e64 s[0:1], 0, v74
	s_nop 1
	v_cndmask_b32_e64 v74, v75, v76, s[0:1]
	v_mul_f32_e32 v75, 0x37800000, v74
	v_cndmask_b32_e32 v74, v74, v75, vcc
	v_cmp_class_f32_e32 vcc, v1, v221
	s_nop 1
	v_cndmask_b32_e32 v1, v74, v1, vcc
	v_div_scale_f32 v74, s[0:1], v1, v1, s74
	v_rcp_f32_e32 v75, v74
	s_nop 0
	v_fma_f32 v76, -v74, v75, 1.0
	v_fmac_f32_e32 v75, v76, v75
	v_div_scale_f32 v76, vcc, s74, v1, s74
	v_mul_f32_e32 v77, v76, v75
	v_fma_f32 v78, -v74, v77, v76
	v_fmac_f32_e32 v77, v78, v75
	v_fma_f32 v74, -v74, v77, v76
	v_div_fmas_f32 v74, v74, v75, v77
	v_div_fixup_f32 v74, v74, v1, s74
	v_pk_mul_f32 v[64:65], v[64:65], v[74:75] op_sel_hi:[1,0]
	v_mov_b32_e32 v76, v3
	v_pk_mul_f32 v[68:69], v[68:69], v[74:75] op_sel_hi:[1,0]
	v_cvt_pk_fp8_f32 v76, v64, v65
	v_mov_b32_e32 v77, v3
	v_pk_mul_f32 v[56:57], v[56:57], v[74:75] op_sel_hi:[1,0]
	v_pk_mul_f32 v[60:61], v[60:61], v[74:75] op_sel_hi:[1,0]
	v_mov_b32_e32 v64, v3
	v_mov_b32_e32 v65, v3
	v_cvt_pk_fp8_f32 v77, v68, v69
	v_cvt_pk_fp8_f32 v64, v56, v57
	v_cvt_pk_fp8_f32 v65, v60, v61
	v_pk_mul_f32 v[66:67], v[66:67], v[74:75] op_sel_hi:[1,0]
	v_pk_mul_f32 v[70:71], v[70:71], v[74:75] op_sel_hi:[1,0]
	v_pk_mul_f32 v[58:59], v[58:59], v[74:75] op_sel_hi:[1,0]
	v_pk_mul_f32 v[62:63], v[62:63], v[74:75] op_sel_hi:[1,0]
	v_cvt_pk_fp8_f32 v76, v66, v67 op_sel:[0,0,1]
	v_cvt_pk_fp8_f32 v77, v70, v71 op_sel:[0,0,1]
	v_cvt_pk_fp8_f32 v64, v58, v59 op_sel:[0,0,1]
	v_cvt_pk_fp8_f32 v65, v62, v63 op_sel:[0,0,1]
	v_add_u32_e32 v56, 0x90, v142
	v_ashrrev_i32_e32 v57, 31, v56
	global_store_dwordx2 v[72:73], v[76:77], off
	global_store_dwordx2 v[72:73], v[64:65], off offset:128
	v_lshlrev_b64 v[58:59], 6, v[56:57]
	v_lshl_add_u64 v[58:59], s[10:11], 0, v[58:59]
	v_lshlrev_b64 v[56:57], 11, v[56:57]
	v_lshl_add_u64 v[56:57], s[8:9], 0, v[56:57]
	v_lshl_add_u64 v[56:57], v[56:57], 0, v[140:141]
	s_waitcnt vmcnt(12)
	v_mov_b32_e32 v58, v172
	v_mov_b32_e32 v59, v173
	v_mov_b32_e32 v60, v174
	v_mov_b32_e32 v61, v175
	v_mov_b32_e32 v62, v59
	v_mov_b32_e32 v63, v60
	v_mov_b32_e32 v59, v61
	v_pk_add_f32 v[58:59], v[62:63], v[58:59]
	s_nop 0
	v_add_f32_e32 v1, v58, v59
	v_add_f32_e32 v1, 0, v1
	v_fmamk_f32 v1, v1, 0x3b800000, v220
	v_cmp_gt_f32_e32 vcc, s93, v1
	v_mul_f32_e32 v58, 0x4f800000, v1
	s_nop 0
	v_cndmask_b32_e32 v1, v1, v58, vcc
	v_sqrt_f32_e32 v58, v1
	s_nop 0
	v_add_u32_e32 v59, -1, v58
	v_fma_f32 v60, -v59, v58, v1
	v_cmp_ge_f32_e64 s[0:1], 0, v60
	v_add_u32_e32 v60, 1, v58
	s_nop 0
	v_cndmask_b32_e64 v59, v58, v59, s[0:1]
	v_fma_f32 v58, -v60, v58, v1
	v_cmp_lt_f32_e64 s[0:1], 0, v58
	s_nop 1
	v_cndmask_b32_e64 v58, v59, v60, s[0:1]
	v_mul_f32_e32 v59, 0x37800000, v58
	v_cndmask_b32_e32 v58, v58, v59, vcc
	v_cmp_class_f32_e32 vcc, v1, v221
	s_nop 1
	v_cndmask_b32_e32 v1, v58, v1, vcc
	v_div_scale_f32 v58, s[0:1], v1, v1, s74
	v_rcp_f32_e32 v59, v58
	s_nop 0
	v_fma_f32 v60, -v58, v59, 1.0
	v_fmac_f32_e32 v59, v60, v59
	v_div_scale_f32 v60, vcc, s74, v1, s74
	v_mul_f32_e32 v61, v60, v59
	v_fma_f32 v62, -v58, v61, v60
	v_fmac_f32_e32 v61, v62, v59
	v_fma_f32 v58, -v58, v61, v60
	v_div_fmas_f32 v58, v58, v59, v61
	v_div_fixup_f32 v58, v58, v1, s74
	v_pk_mul_f32 v[48:49], v[48:49], v[58:59] op_sel_hi:[1,0]
	v_mov_b32_e32 v60, v3
	v_pk_mul_f32 v[52:53], v[52:53], v[58:59] op_sel_hi:[1,0]
	v_cvt_pk_fp8_f32 v60, v48, v49
	v_mov_b32_e32 v61, v3
	v_pk_mul_f32 v[40:41], v[40:41], v[58:59] op_sel_hi:[1,0]
	v_pk_mul_f32 v[44:45], v[44:45], v[58:59] op_sel_hi:[1,0]
	v_mov_b32_e32 v48, v3
	v_mov_b32_e32 v49, v3
	v_cvt_pk_fp8_f32 v61, v52, v53
	v_cvt_pk_fp8_f32 v48, v40, v41
	v_cvt_pk_fp8_f32 v49, v44, v45
	v_pk_mul_f32 v[50:51], v[50:51], v[58:59] op_sel_hi:[1,0]
	v_pk_mul_f32 v[54:55], v[54:55], v[58:59] op_sel_hi:[1,0]
	v_pk_mul_f32 v[42:43], v[42:43], v[58:59] op_sel_hi:[1,0]
	v_pk_mul_f32 v[46:47], v[46:47], v[58:59] op_sel_hi:[1,0]
	v_cvt_pk_fp8_f32 v60, v50, v51 op_sel:[0,0,1]
	v_cvt_pk_fp8_f32 v61, v54, v55 op_sel:[0,0,1]
	v_cvt_pk_fp8_f32 v48, v42, v43 op_sel:[0,0,1]
	v_cvt_pk_fp8_f32 v49, v46, v47 op_sel:[0,0,1]
	v_add_u32_e32 v40, 0xa0, v142
	v_ashrrev_i32_e32 v41, 31, v40
	global_store_dwordx2 v[56:57], v[60:61], off
	global_store_dwordx2 v[56:57], v[48:49], off offset:128
	v_lshlrev_b64 v[42:43], 6, v[40:41]
	v_lshl_add_u64 v[42:43], s[10:11], 0, v[42:43]
	v_lshlrev_b64 v[40:41], 11, v[40:41]
	v_lshl_add_u64 v[40:41], s[8:9], 0, v[40:41]
	v_lshl_add_u64 v[40:41], v[40:41], 0, v[140:141]
	s_waitcnt vmcnt(13)
	v_mov_b32_e32 v42, v176
	v_mov_b32_e32 v43, v177
	v_mov_b32_e32 v44, v178
	v_mov_b32_e32 v45, v179
	v_mov_b32_e32 v46, v43
	v_mov_b32_e32 v47, v44
	v_mov_b32_e32 v43, v45
	v_pk_add_f32 v[42:43], v[46:47], v[42:43]
	s_nop 0
	v_add_f32_e32 v1, v42, v43
	v_add_f32_e32 v1, 0, v1
	v_fmamk_f32 v1, v1, 0x3b800000, v220
	v_cmp_gt_f32_e32 vcc, s93, v1
	v_mul_f32_e32 v42, 0x4f800000, v1
	s_nop 0
	v_cndmask_b32_e32 v1, v1, v42, vcc
	v_sqrt_f32_e32 v42, v1
	s_nop 0
	v_add_u32_e32 v43, -1, v42
	v_fma_f32 v44, -v43, v42, v1
	v_cmp_ge_f32_e64 s[0:1], 0, v44
	v_add_u32_e32 v44, 1, v42
	s_nop 0
	v_cndmask_b32_e64 v43, v42, v43, s[0:1]
	v_fma_f32 v42, -v44, v42, v1
	v_cmp_lt_f32_e64 s[0:1], 0, v42
	s_nop 1
	v_cndmask_b32_e64 v42, v43, v44, s[0:1]
	v_mul_f32_e32 v43, 0x37800000, v42
	v_cndmask_b32_e32 v42, v42, v43, vcc
	v_cmp_class_f32_e32 vcc, v1, v221
	s_nop 1
	v_cndmask_b32_e32 v1, v42, v1, vcc
	v_div_scale_f32 v42, s[0:1], v1, v1, s74
	v_rcp_f32_e32 v43, v42
	s_nop 0
	v_fma_f32 v44, -v42, v43, 1.0
	v_fmac_f32_e32 v43, v44, v43
	v_div_scale_f32 v44, vcc, s74, v1, s74
	v_mul_f32_e32 v45, v44, v43
	v_fma_f32 v46, -v42, v45, v44
	v_fmac_f32_e32 v45, v46, v43
	v_fma_f32 v42, -v42, v45, v44
	v_div_fmas_f32 v42, v42, v43, v45
	v_div_fixup_f32 v42, v42, v1, s74
	v_pk_mul_f32 v[32:33], v[32:33], v[42:43] op_sel_hi:[1,0]
	v_mov_b32_e32 v44, v3
	v_pk_mul_f32 v[36:37], v[36:37], v[42:43] op_sel_hi:[1,0]
	v_cvt_pk_fp8_f32 v44, v32, v33
	v_mov_b32_e32 v45, v3
	v_pk_mul_f32 v[24:25], v[24:25], v[42:43] op_sel_hi:[1,0]
	v_pk_mul_f32 v[28:29], v[28:29], v[42:43] op_sel_hi:[1,0]
	v_mov_b32_e32 v32, v3
	v_mov_b32_e32 v33, v3
	v_cvt_pk_fp8_f32 v45, v36, v37
	v_cvt_pk_fp8_f32 v32, v24, v25
	v_cvt_pk_fp8_f32 v33, v28, v29
	v_pk_mul_f32 v[34:35], v[34:35], v[42:43] op_sel_hi:[1,0]
	v_pk_mul_f32 v[38:39], v[38:39], v[42:43] op_sel_hi:[1,0]
	v_pk_mul_f32 v[26:27], v[26:27], v[42:43] op_sel_hi:[1,0]
	v_pk_mul_f32 v[30:31], v[30:31], v[42:43] op_sel_hi:[1,0]
	v_cvt_pk_fp8_f32 v44, v34, v35 op_sel:[0,0,1]
	v_cvt_pk_fp8_f32 v45, v38, v39 op_sel:[0,0,1]
	v_cvt_pk_fp8_f32 v32, v26, v27 op_sel:[0,0,1]
	v_cvt_pk_fp8_f32 v33, v30, v31 op_sel:[0,0,1]
	v_add_u32_e32 v24, 0xb0, v142
	v_ashrrev_i32_e32 v25, 31, v24
	global_store_dwordx2 v[40:41], v[44:45], off
	global_store_dwordx2 v[40:41], v[32:33], off offset:128
	v_lshlrev_b64 v[26:27], 6, v[24:25]
	v_lshl_add_u64 v[26:27], s[10:11], 0, v[26:27]
	v_lshlrev_b64 v[24:25], 11, v[24:25]
	v_lshl_add_u64 v[24:25], s[8:9], 0, v[24:25]
	v_lshl_add_u64 v[24:25], v[24:25], 0, v[140:141]
	s_waitcnt vmcnt(14)
	v_mov_b32_e32 v26, v180
	v_mov_b32_e32 v27, v181
	v_mov_b32_e32 v28, v182
	v_mov_b32_e32 v29, v183
	v_mov_b32_e32 v30, v27
	v_mov_b32_e32 v31, v28
	v_mov_b32_e32 v27, v29
	v_pk_add_f32 v[26:27], v[30:31], v[26:27]
	s_nop 0
	v_add_f32_e32 v1, v26, v27
	v_add_f32_e32 v1, 0, v1
	v_fmamk_f32 v1, v1, 0x3b800000, v220
	v_cmp_gt_f32_e32 vcc, s93, v1
	v_mul_f32_e32 v26, 0x4f800000, v1
	s_nop 0
	v_cndmask_b32_e32 v1, v1, v26, vcc
	v_sqrt_f32_e32 v26, v1
	s_nop 0
	v_add_u32_e32 v27, -1, v26
	v_fma_f32 v28, -v27, v26, v1
	v_cmp_ge_f32_e64 s[0:1], 0, v28
	v_add_u32_e32 v28, 1, v26
	s_nop 0
	v_cndmask_b32_e64 v27, v26, v27, s[0:1]
	v_fma_f32 v26, -v28, v26, v1
	v_cmp_lt_f32_e64 s[0:1], 0, v26
	s_nop 1
	v_cndmask_b32_e64 v26, v27, v28, s[0:1]
	v_mul_f32_e32 v27, 0x37800000, v26
	v_cndmask_b32_e32 v26, v26, v27, vcc
	v_cmp_class_f32_e32 vcc, v1, v221
	s_nop 1
	v_cndmask_b32_e32 v1, v26, v1, vcc
	v_div_scale_f32 v26, s[0:1], v1, v1, s74
	v_rcp_f32_e32 v27, v26
	s_mov_b64 s[0:1], -1
	v_fma_f32 v28, -v26, v27, 1.0
	v_fmac_f32_e32 v27, v28, v27
	v_div_scale_f32 v28, vcc, s74, v1, s74
	v_mul_f32_e32 v29, v28, v27
	v_fma_f32 v30, -v26, v29, v28
	v_fmac_f32_e32 v29, v30, v27
	v_fma_f32 v26, -v26, v29, v28
	v_div_fmas_f32 v26, v26, v27, v29
	v_div_fixup_f32 v26, v26, v1, s74
	v_pk_mul_f32 v[12:13], v[12:13], v[26:27] op_sel_hi:[1,0]
	v_mov_b32_e32 v28, v3
	v_pk_mul_f32 v[20:21], v[20:21], v[26:27] op_sel_hi:[1,0]
	v_cvt_pk_fp8_f32 v28, v12, v13
	v_mov_b32_e32 v29, v3
	v_pk_mul_f32 v[8:9], v[8:9], v[26:27] op_sel_hi:[1,0]
	v_pk_mul_f32 v[4:5], v[4:5], v[26:27] op_sel_hi:[1,0]
	v_mov_b32_e32 v12, v3
	v_mov_b32_e32 v13, v3
	v_cvt_pk_fp8_f32 v29, v20, v21
	v_cvt_pk_fp8_f32 v12, v8, v9
	v_cvt_pk_fp8_f32 v13, v4, v5
	v_pk_mul_f32 v[14:15], v[14:15], v[26:27] op_sel_hi:[1,0]
	v_pk_mul_f32 v[22:23], v[22:23], v[26:27] op_sel_hi:[1,0]
	v_pk_mul_f32 v[10:11], v[10:11], v[26:27] op_sel_hi:[1,0]
	v_pk_mul_f32 v[6:7], v[6:7], v[26:27] op_sel_hi:[1,0]
	v_cvt_pk_fp8_f32 v28, v14, v15 op_sel:[0,0,1]
	v_cvt_pk_fp8_f32 v29, v22, v23 op_sel:[0,0,1]
	v_cvt_pk_fp8_f32 v12, v10, v11 op_sel:[0,0,1]
	v_cvt_pk_fp8_f32 v13, v6, v7 op_sel:[0,0,1]
	s_andn2_b64 vcc, exec, s[6:7]
	global_store_dwordx2 v[24:25], v[28:29], off
	global_store_dwordx2 v[24:25], v[12:13], off offset:128
	s_cbranch_vccnz .LBB0_482
	s_andn2_b64 vcc, exec, s[4:5]
	s_cbranch_vccnz .LBB0_481
	s_barrier
	s_branch .LBB0_481

.LBB0_507:
	s_lshl_b32 s0, s0, 8
	v_mov_b32_e32 v1, v0
	s_add_i32 s0, s0, s54
	s_nop 15
	s_nop 7
	v_mov_b32_e32 v30, v3
	v_and_or_b32 v8, v1, 15, s0
	v_ashrrev_i32_e32 v9, 31, v8
	v_lshlrev_b64 v[6:7], 6, v[8:9]
	v_lshl_add_u64 v[6:7], s[10:11], 0, v[6:7]
	global_load_dwordx4 v[20:23], v[6:7], off
	global_load_dwordx4 v[24:27], v[6:7], off offset:16
	global_load_dwordx4 v[32:35], v[6:7], off offset:1024
	global_load_dwordx4 v[36:39], v[6:7], off offset:1040
	global_load_dwordx4 v[40:43], v[6:7], off offset:2048
	global_load_dwordx4 v[172:175], v[6:7], off offset:2064
	global_load_dwordx4 v[176:179], v[6:7], off offset:3072
	global_load_dwordx4 v[182:185], v[6:7], off offset:3088
	s_mov_b64 vcc, 0x2000
	v_lshl_add_u64 v[234:235], v[6:7], 0, vcc
	global_load_dwordx4 v[186:189], v[234:235], off
	global_load_dwordx4 v[190:193], v[234:235], off offset:16
	global_load_dwordx4 v[194:197], v[234:235], off offset:1024
	global_load_dwordx4 v[204:207], v[234:235], off offset:1040
	global_load_dwordx4 v[208:211], v[234:235], off offset:2048
	global_load_dwordx4 v[230:233], v[234:235], off offset:2064
	s_lshl_b32 s0, s1, 8
	v_lshrrev_b32_e32 v1, 1, v1
	v_and_or_b32 v1, v1, 24, s0
	v_or_b32_e32 v4, s55, v1
	v_mov_b32_e32 v31, v3
	s_movk_i32 s2, 0x600
	v_ashrrev_i32_e32 v5, 31, v4
	s_waitcnt vmcnt(12)
	v_mov_b32_e32 v6, v20
	v_mov_b32_e32 v7, v24
	v_mov_b32_e32 v24, v21
	v_mov_b32_e32 v10, v22
	v_mov_b32_e32 v11, v26
	v_mov_b32_e32 v26, v23
	v_pk_add_f32 v[6:7], v[6:7], v[24:25]
	v_pk_add_f32 v[10:11], v[10:11], v[26:27]
	s_nop 0
	v_pk_add_f32 v[6:7], v[6:7], v[10:11]
	s_nop 0
	v_add_f32_e32 v1, 0, v6
	v_add_f32_e32 v1, v1, v7
	v_fmamk_f32 v1, v1, 0x3b000000, v220
	v_cmp_gt_f32_e32 vcc, s93, v1
	v_mul_f32_e32 v6, 0x4f800000, v1
	s_nop 0
	v_cndmask_b32_e32 v1, v1, v6, vcc
	v_sqrt_f32_e32 v6, v1
	s_nop 0
	v_add_u32_e32 v7, -1, v6
	v_fma_f32 v9, -v7, v6, v1
	v_cmp_ge_f32_e64 s[0:1], 0, v9
	v_add_u32_e32 v9, 1, v6
	s_nop 0
	v_cndmask_b32_e64 v7, v6, v7, s[0:1]
	v_fma_f32 v6, -v9, v6, v1
	v_cmp_lt_f32_e64 s[0:1], 0, v6
	s_nop 1
	v_cndmask_b32_e64 v6, v7, v9, s[0:1]
	v_mul_f32_e32 v7, 0x37800000, v6
	v_cndmask_b32_e32 v6, v6, v7, vcc
	v_cmp_class_f32_e32 vcc, v1, v221
	s_nop 1
	v_cndmask_b32_e32 v1, v6, v1, vcc
	v_div_scale_f32 v6, s[0:1], v1, v1, s74
	v_rcp_f32_e32 v7, v6
	s_nop 0
	v_fma_f32 v9, -v6, v7, 1.0
	v_fmac_f32_e32 v7, v9, v7
	v_div_scale_f32 v9, vcc, s74, v1, s74
	v_mul_f32_e32 v10, v9, v7
	v_fma_f32 v11, -v6, v10, v9
	v_fmac_f32_e32 v10, v11, v7
	v_fma_f32 v6, -v6, v10, v9
	v_div_fmas_f32 v6, v6, v7, v10
	v_div_fixup_f32 v10, v6, v1, s74
	v_pk_mul_f32 v[24:25], v[164:165], v[10:11] op_sel_hi:[1,0]
	v_pk_mul_f32 v[28:29], v[160:161], v[10:11] op_sel_hi:[1,0]
	v_cvt_pk_fp8_f32 v30, v24, v25
	v_cvt_pk_fp8_f32 v31, v28, v29
	v_pk_mul_f32 v[22:23], v[166:167], v[10:11] op_sel_hi:[1,0]
	v_pk_mul_f32 v[26:27], v[162:163], v[10:11] op_sel_hi:[1,0]
	v_cvt_pk_fp8_f32 v30, v22, v23 op_sel:[0,0,1]
	v_cvt_pk_fp8_f32 v31, v26, v27 op_sel:[0,0,1]
	v_pk_mul_f32 v[22:23], v[158:159], v[10:11] op_sel_hi:[1,0]
	v_pk_mul_f32 v[24:25], v[156:157], v[10:11] op_sel_hi:[1,0]
	v_pk_mul_f32 v[26:27], v[154:155], v[10:11] op_sel_hi:[1,0]
	v_pk_mul_f32 v[10:11], v[152:153], v[10:11] op_sel_hi:[1,0]
	v_mov_b32_e32 v28, v3
	v_mov_b32_e32 v29, v3
	v_cvt_pk_fp8_f32 v28, v24, v25
	v_cvt_pk_fp8_f32 v29, v10, v11
	v_mov_b64_e32 v[6:7], s[8:9]
	v_mad_i64_i32 v[20:21], s[0:1], v8, s2, v[6:7]
	v_cvt_pk_fp8_f32 v28, v22, v23 op_sel:[0,0,1]
	v_cvt_pk_fp8_f32 v29, v26, v27 op_sel:[0,0,1]
	v_or_b32_e32 v10, 16, v8
	v_lshl_add_u64 v[20:21], v[20:21], 0, v[4:5]
	v_ashrrev_i32_e32 v11, 31, v10
	global_store_dwordx2 v[20:21], v[30:31], off
	global_store_dwordx2 v[20:21], v[28:29], off offset:128
	v_lshlrev_b64 v[20:21], 6, v[10:11]
	v_lshl_add_u64 v[24:25], s[10:11], 0, v[20:21]
	s_nop 0
	v_mov_b32_e32 v30, v3
	v_mov_b32_e32 v31, v3
	s_waitcnt vmcnt(12)
	v_mov_b32_e32 v20, v32
	v_mov_b32_e32 v21, v33
	v_mov_b32_e32 v22, v34
	v_mov_b32_e32 v23, v35
	v_mov_b32_e32 v24, v36
	v_mov_b32_e32 v25, v37
	v_mov_b32_e32 v26, v38
	v_mov_b32_e32 v27, v39
	v_mov_b32_e32 v28, v20
	v_mov_b32_e32 v29, v24
	v_mov_b32_e32 v24, v21
	v_pk_add_f32 v[20:21], v[28:29], v[24:25]
	v_mov_b32_e32 v24, v22
	v_mov_b32_e32 v25, v26
	v_mov_b32_e32 v26, v23
	v_pk_add_f32 v[22:23], v[24:25], v[26:27]
	s_nop 0
	v_pk_add_f32 v[20:21], v[20:21], v[22:23]
	s_nop 0
	v_add_f32_e32 v1, 0, v20
	v_add_f32_e32 v1, v1, v21
	v_fmamk_f32 v1, v1, 0x3b000000, v220
	v_cmp_gt_f32_e32 vcc, s93, v1
	v_mul_f32_e32 v9, 0x4f800000, v1
	s_nop 0
	v_cndmask_b32_e32 v1, v1, v9, vcc
	v_sqrt_f32_e32 v9, v1
	s_nop 0
	v_add_u32_e32 v11, -1, v9
	v_fma_f32 v20, -v11, v9, v1
	v_cmp_ge_f32_e64 s[0:1], 0, v20
	v_add_u32_e32 v20, 1, v9
	s_nop 0
	v_cndmask_b32_e64 v11, v9, v11, s[0:1]
	v_fma_f32 v9, -v20, v9, v1
	v_cmp_lt_f32_e64 s[0:1], 0, v9
	s_nop 1
	v_cndmask_b32_e64 v9, v11, v20, s[0:1]
	v_mul_f32_e32 v11, 0x37800000, v9
	v_cndmask_b32_e32 v9, v9, v11, vcc
	v_cmp_class_f32_e32 vcc, v1, v221
	s_nop 1
	v_cndmask_b32_e32 v1, v9, v1, vcc
	v_div_scale_f32 v9, s[0:1], v1, v1, s74
	v_rcp_f32_e32 v11, v9
	s_nop 0
	v_fma_f32 v20, -v9, v11, 1.0
	v_fmac_f32_e32 v11, v20, v11
	v_div_scale_f32 v20, vcc, s74, v1, s74
	v_mul_f32_e32 v21, v20, v11
	v_fma_f32 v22, -v9, v21, v20
	v_fmac_f32_e32 v21, v22, v11
	v_fma_f32 v9, -v9, v21, v20
	v_div_fmas_f32 v9, v9, v11, v21
	v_div_fixup_f32 v20, v9, v1, s74
	v_pk_mul_f32 v[24:25], v[148:149], v[20:21] op_sel_hi:[1,0]
	v_pk_mul_f32 v[28:29], v[144:145], v[20:21] op_sel_hi:[1,0]
	v_cvt_pk_fp8_f32 v30, v24, v25
	v_cvt_pk_fp8_f32 v31, v28, v29
	v_pk_mul_f32 v[22:23], v[150:151], v[20:21] op_sel_hi:[1,0]
	v_pk_mul_f32 v[26:27], v[146:147], v[20:21] op_sel_hi:[1,0]
	v_cvt_pk_fp8_f32 v30, v22, v23 op_sel:[0,0,1]
	v_cvt_pk_fp8_f32 v31, v26, v27 op_sel:[0,0,1]
	v_pk_mul_f32 v[22:23], v[142:143], v[20:21] op_sel_hi:[1,0]
	v_pk_mul_f32 v[24:25], v[140:141], v[20:21] op_sel_hi:[1,0]
	v_pk_mul_f32 v[26:27], v[138:139], v[20:21] op_sel_hi:[1,0]
	v_pk_mul_f32 v[20:21], v[136:137], v[20:21] op_sel_hi:[1,0]
	v_mov_b32_e32 v28, v3
	v_mov_b32_e32 v29, v3
	v_cvt_pk_fp8_f32 v28, v24, v25
	v_cvt_pk_fp8_f32 v29, v20, v21
	v_mad_i64_i32 v[10:11], s[0:1], v10, s2, v[6:7]
	v_cvt_pk_fp8_f32 v28, v22, v23 op_sel:[0,0,1]
	v_cvt_pk_fp8_f32 v29, v26, v27 op_sel:[0,0,1]
	v_lshl_add_u64 v[10:11], v[10:11], 0, v[4:5]
	global_store_dwordx2 v[10:11], v[30:31], off
	v_mov_b32_e32 v30, v3
	global_store_dwordx2 v[10:11], v[28:29], off offset:128
	v_or_b32_e32 v10, 32, v8
	v_ashrrev_i32_e32 v11, 31, v10
	v_lshlrev_b64 v[20:21], 6, v[10:11]
	v_lshl_add_u64 v[24:25], s[10:11], 0, v[20:21]
	s_nop 0
	v_mov_b32_e32 v31, v3
	s_waitcnt vmcnt(12)
	v_mov_b32_e32 v20, v40
	v_mov_b32_e32 v21, v41
	v_mov_b32_e32 v22, v42
	v_mov_b32_e32 v23, v43
	v_mov_b32_e32 v24, v172
	v_mov_b32_e32 v25, v173
	v_mov_b32_e32 v26, v174
	v_mov_b32_e32 v27, v175
	v_mov_b32_e32 v28, v20
	v_mov_b32_e32 v29, v24
	v_mov_b32_e32 v24, v21
	v_pk_add_f32 v[20:21], v[28:29], v[24:25]
	v_mov_b32_e32 v24, v22
	v_mov_b32_e32 v25, v26
	v_mov_b32_e32 v26, v23
	v_pk_add_f32 v[22:23], v[24:25], v[26:27]
	s_nop 0
	v_pk_add_f32 v[20:21], v[20:21], v[22:23]
	s_nop 0
	v_add_f32_e32 v1, 0, v20
	v_add_f32_e32 v1, v1, v21
	v_fmamk_f32 v1, v1, 0x3b000000, v220
	v_cmp_gt_f32_e32 vcc, s93, v1
	v_mul_f32_e32 v9, 0x4f800000, v1
	s_nop 0
	v_cndmask_b32_e32 v1, v1, v9, vcc
	v_sqrt_f32_e32 v9, v1
	s_nop 0
	v_add_u32_e32 v11, -1, v9
	v_fma_f32 v20, -v11, v9, v1
	v_cmp_ge_f32_e64 s[0:1], 0, v20
	v_add_u32_e32 v20, 1, v9
	s_nop 0
	v_cndmask_b32_e64 v11, v9, v11, s[0:1]
	v_fma_f32 v9, -v20, v9, v1
	v_cmp_lt_f32_e64 s[0:1], 0, v9
	s_nop 1
	v_cndmask_b32_e64 v9, v11, v20, s[0:1]
	v_mul_f32_e32 v11, 0x37800000, v9
	v_cndmask_b32_e32 v9, v9, v11, vcc
	v_cmp_class_f32_e32 vcc, v1, v221
	s_nop 1
	v_cndmask_b32_e32 v1, v9, v1, vcc
	v_div_scale_f32 v9, s[0:1], v1, v1, s74
	v_rcp_f32_e32 v11, v9
	s_nop 0
	v_fma_f32 v20, -v9, v11, 1.0
	v_fmac_f32_e32 v11, v20, v11
	v_div_scale_f32 v20, vcc, s74, v1, s74
	v_mul_f32_e32 v21, v20, v11
	v_fma_f32 v22, -v9, v21, v20
	v_fmac_f32_e32 v21, v22, v11
	v_fma_f32 v9, -v9, v21, v20
	v_div_fmas_f32 v9, v9, v11, v21
	v_div_fixup_f32 v20, v9, v1, s74
	v_pk_mul_f32 v[24:25], v[132:133], v[20:21] op_sel_hi:[1,0]
	v_pk_mul_f32 v[28:29], v[128:129], v[20:21] op_sel_hi:[1,0]
	v_cvt_pk_fp8_f32 v30, v24, v25
	v_cvt_pk_fp8_f32 v31, v28, v29
	v_pk_mul_f32 v[22:23], v[134:135], v[20:21] op_sel_hi:[1,0]
	v_pk_mul_f32 v[26:27], v[130:131], v[20:21] op_sel_hi:[1,0]
	v_cvt_pk_fp8_f32 v30, v22, v23 op_sel:[0,0,1]
	v_cvt_pk_fp8_f32 v31, v26, v27 op_sel:[0,0,1]
	v_pk_mul_f32 v[22:23], v[126:127], v[20:21] op_sel_hi:[1,0]
	v_pk_mul_f32 v[24:25], v[124:125], v[20:21] op_sel_hi:[1,0]
	v_pk_mul_f32 v[26:27], v[122:123], v[20:21] op_sel_hi:[1,0]
	v_pk_mul_f32 v[20:21], v[120:121], v[20:21] op_sel_hi:[1,0]
	v_mov_b32_e32 v28, v3
	v_mov_b32_e32 v29, v3
	v_cvt_pk_fp8_f32 v28, v24, v25
	v_cvt_pk_fp8_f32 v29, v20, v21
	v_mad_i64_i32 v[10:11], s[0:1], v10, s2, v[6:7]
	v_cvt_pk_fp8_f32 v28, v22, v23 op_sel:[0,0,1]
	v_cvt_pk_fp8_f32 v29, v26, v27 op_sel:[0,0,1]
	v_lshl_add_u64 v[10:11], v[10:11], 0, v[4:5]
	global_store_dwordx2 v[10:11], v[30:31], off
	v_mov_b32_e32 v30, v3
	global_store_dwordx2 v[10:11], v[28:29], off offset:128
	v_or_b32_e32 v10, 48, v8
	v_ashrrev_i32_e32 v11, 31, v10
	v_lshlrev_b64 v[20:21], 6, v[10:11]
	v_lshl_add_u64 v[24:25], s[10:11], 0, v[20:21]
	s_nop 0
	v_mov_b32_e32 v31, v3
	s_waitcnt vmcnt(12)
	v_mov_b32_e32 v20, v176
	v_mov_b32_e32 v21, v177
	v_mov_b32_e32 v22, v178
	v_mov_b32_e32 v23, v179
	v_mov_b32_e32 v24, v182
	v_mov_b32_e32 v25, v183
	v_mov_b32_e32 v26, v184
	v_mov_b32_e32 v27, v185
	v_mov_b32_e32 v28, v20
	v_mov_b32_e32 v29, v24
	v_mov_b32_e32 v24, v21
	v_pk_add_f32 v[20:21], v[28:29], v[24:25]
	v_mov_b32_e32 v24, v22
	v_mov_b32_e32 v25, v26
	v_mov_b32_e32 v26, v23
	v_pk_add_f32 v[22:23], v[24:25], v[26:27]
	s_nop 0
	v_pk_add_f32 v[20:21], v[20:21], v[22:23]
	s_nop 0
	v_add_f32_e32 v1, 0, v20
	v_add_f32_e32 v1, v1, v21
	v_fmamk_f32 v1, v1, 0x3b000000, v220
	v_cmp_gt_f32_e32 vcc, s93, v1
	v_mul_f32_e32 v9, 0x4f800000, v1
	s_nop 0
	v_cndmask_b32_e32 v1, v1, v9, vcc
	v_sqrt_f32_e32 v9, v1
	s_nop 0
	v_add_u32_e32 v11, -1, v9
	v_fma_f32 v20, -v11, v9, v1
	v_cmp_ge_f32_e64 s[0:1], 0, v20
	v_add_u32_e32 v20, 1, v9
	s_nop 0
	v_cndmask_b32_e64 v11, v9, v11, s[0:1]
	v_fma_f32 v9, -v20, v9, v1
	v_cmp_lt_f32_e64 s[0:1], 0, v9
	s_nop 1
	v_cndmask_b32_e64 v9, v11, v20, s[0:1]
	v_mul_f32_e32 v11, 0x37800000, v9
	v_cndmask_b32_e32 v9, v9, v11, vcc
	v_cmp_class_f32_e32 vcc, v1, v221
	s_nop 1
	v_cndmask_b32_e32 v1, v9, v1, vcc
	v_div_scale_f32 v9, s[0:1], v1, v1, s74
	v_rcp_f32_e32 v11, v9
	s_nop 0
	v_fma_f32 v20, -v9, v11, 1.0
	v_fmac_f32_e32 v11, v20, v11
	v_div_scale_f32 v20, vcc, s74, v1, s74
	v_mul_f32_e32 v21, v20, v11
	v_fma_f32 v22, -v9, v21, v20
	v_fmac_f32_e32 v21, v22, v11
	v_fma_f32 v9, -v9, v21, v20
	v_div_fmas_f32 v9, v9, v11, v21
	v_div_fixup_f32 v20, v9, v1, s74
	v_pk_mul_f32 v[24:25], v[116:117], v[20:21] op_sel_hi:[1,0]
	v_pk_mul_f32 v[28:29], v[112:113], v[20:21] op_sel_hi:[1,0]
	v_cvt_pk_fp8_f32 v30, v24, v25
	v_cvt_pk_fp8_f32 v31, v28, v29
	v_pk_mul_f32 v[22:23], v[118:119], v[20:21] op_sel_hi:[1,0]
	v_pk_mul_f32 v[26:27], v[114:115], v[20:21] op_sel_hi:[1,0]
	v_cvt_pk_fp8_f32 v30, v22, v23 op_sel:[0,0,1]
	v_cvt_pk_fp8_f32 v31, v26, v27 op_sel:[0,0,1]
	v_pk_mul_f32 v[22:23], v[110:111], v[20:21] op_sel_hi:[1,0]
	v_pk_mul_f32 v[24:25], v[108:109], v[20:21] op_sel_hi:[1,0]
	v_pk_mul_f32 v[26:27], v[106:107], v[20:21] op_sel_hi:[1,0]
	v_pk_mul_f32 v[20:21], v[104:105], v[20:21] op_sel_hi:[1,0]
	v_mov_b32_e32 v28, v3
	v_mov_b32_e32 v29, v3
	v_cvt_pk_fp8_f32 v28, v24, v25
	v_cvt_pk_fp8_f32 v29, v20, v21
	v_mad_i64_i32 v[10:11], s[0:1], v10, s2, v[6:7]
	v_cvt_pk_fp8_f32 v28, v22, v23 op_sel:[0,0,1]
	v_cvt_pk_fp8_f32 v29, v26, v27 op_sel:[0,0,1]
	v_lshl_add_u64 v[10:11], v[10:11], 0, v[4:5]
	global_store_dwordx2 v[10:11], v[30:31], off
	v_mov_b32_e32 v30, v3
	global_store_dwordx2 v[10:11], v[28:29], off offset:128
	v_add_u32_e32 v10, 0x80, v8
	v_ashrrev_i32_e32 v11, 31, v10
	v_lshlrev_b64 v[20:21], 6, v[10:11]
	v_lshl_add_u64 v[24:25], s[10:11], 0, v[20:21]
	s_nop 0
	v_mov_b32_e32 v31, v3
	s_waitcnt vmcnt(12)
	v_mov_b32_e32 v20, v186
	v_mov_b32_e32 v21, v187
	v_mov_b32_e32 v22, v188
	v_mov_b32_e32 v23, v189
	v_mov_b32_e32 v24, v190
	v_mov_b32_e32 v25, v191
	v_mov_b32_e32 v26, v192
	v_mov_b32_e32 v27, v193
	v_mov_b32_e32 v28, v20
	v_mov_b32_e32 v29, v24
	v_mov_b32_e32 v24, v21
	v_pk_add_f32 v[20:21], v[28:29], v[24:25]
	v_mov_b32_e32 v24, v22
	v_mov_b32_e32 v25, v26
	v_mov_b32_e32 v26, v23
	v_pk_add_f32 v[22:23], v[24:25], v[26:27]
	s_nop 0
	v_pk_add_f32 v[20:21], v[20:21], v[22:23]
	s_nop 0
	v_add_f32_e32 v1, 0, v20
	v_add_f32_e32 v1, v1, v21
	v_fmamk_f32 v1, v1, 0x3b000000, v220
	v_cmp_gt_f32_e32 vcc, s93, v1
	v_mul_f32_e32 v9, 0x4f800000, v1
	s_nop 0
	v_cndmask_b32_e32 v1, v1, v9, vcc
	v_sqrt_f32_e32 v9, v1
	s_nop 0
	v_add_u32_e32 v11, -1, v9
	v_fma_f32 v20, -v11, v9, v1
	v_cmp_ge_f32_e64 s[0:1], 0, v20
	v_add_u32_e32 v20, 1, v9
	s_nop 0
	v_cndmask_b32_e64 v11, v9, v11, s[0:1]
	v_fma_f32 v9, -v20, v9, v1
	v_cmp_lt_f32_e64 s[0:1], 0, v9
	s_nop 1
	v_cndmask_b32_e64 v9, v11, v20, s[0:1]
	v_mul_f32_e32 v11, 0x37800000, v9
	v_cndmask_b32_e32 v9, v9, v11, vcc
	v_cmp_class_f32_e32 vcc, v1, v221
	s_nop 1
	v_cndmask_b32_e32 v1, v9, v1, vcc
	v_div_scale_f32 v9, s[0:1], v1, v1, s74
	v_rcp_f32_e32 v11, v9
	s_nop 0
	v_fma_f32 v20, -v9, v11, 1.0
	v_fmac_f32_e32 v11, v20, v11
	v_div_scale_f32 v20, vcc, s74, v1, s74
	v_mul_f32_e32 v21, v20, v11
	v_fma_f32 v22, -v9, v21, v20
	v_fmac_f32_e32 v21, v22, v11
	v_fma_f32 v9, -v9, v21, v20
	v_div_fmas_f32 v9, v9, v11, v21
	v_div_fixup_f32 v20, v9, v1, s74
	v_pk_mul_f32 v[24:25], v[100:101], v[20:21] op_sel_hi:[1,0]
	v_pk_mul_f32 v[28:29], v[96:97], v[20:21] op_sel_hi:[1,0]
	v_cvt_pk_fp8_f32 v30, v24, v25
	v_cvt_pk_fp8_f32 v31, v28, v29
	v_pk_mul_f32 v[22:23], v[102:103], v[20:21] op_sel_hi:[1,0]
	v_pk_mul_f32 v[26:27], v[98:99], v[20:21] op_sel_hi:[1,0]
	v_cvt_pk_fp8_f32 v30, v22, v23 op_sel:[0,0,1]
	v_cvt_pk_fp8_f32 v31, v26, v27 op_sel:[0,0,1]
	v_pk_mul_f32 v[22:23], v[94:95], v[20:21] op_sel_hi:[1,0]
	v_pk_mul_f32 v[24:25], v[92:93], v[20:21] op_sel_hi:[1,0]
	v_pk_mul_f32 v[26:27], v[90:91], v[20:21] op_sel_hi:[1,0]
	v_pk_mul_f32 v[20:21], v[88:89], v[20:21] op_sel_hi:[1,0]
	v_mov_b32_e32 v28, v3
	v_mov_b32_e32 v29, v3
	v_cvt_pk_fp8_f32 v28, v24, v25
	v_cvt_pk_fp8_f32 v29, v20, v21
	v_mad_i64_i32 v[10:11], s[0:1], v10, s2, v[6:7]
	v_cvt_pk_fp8_f32 v28, v22, v23 op_sel:[0,0,1]
	v_cvt_pk_fp8_f32 v29, v26, v27 op_sel:[0,0,1]
	v_lshl_add_u64 v[10:11], v[10:11], 0, v[4:5]
	global_store_dwordx2 v[10:11], v[30:31], off
	v_mov_b32_e32 v30, v3
	global_store_dwordx2 v[10:11], v[28:29], off offset:128
	v_add_u32_e32 v10, 0x90, v8
	v_ashrrev_i32_e32 v11, 31, v10
	v_lshlrev_b64 v[20:21], 6, v[10:11]
	v_lshl_add_u64 v[24:25], s[10:11], 0, v[20:21]
	s_nop 0
	v_mov_b32_e32 v31, v3
	s_waitcnt vmcnt(12)
	v_mov_b32_e32 v20, v194
	v_mov_b32_e32 v21, v195
	v_mov_b32_e32 v22, v196
	v_mov_b32_e32 v23, v197
	v_mov_b32_e32 v24, v204
	v_mov_b32_e32 v25, v205
	v_mov_b32_e32 v26, v206
	v_mov_b32_e32 v27, v207
	v_mov_b32_e32 v28, v20
	v_mov_b32_e32 v29, v24
	v_mov_b32_e32 v24, v21
	v_pk_add_f32 v[20:21], v[28:29], v[24:25]
	v_mov_b32_e32 v24, v22
	v_mov_b32_e32 v25, v26
	v_mov_b32_e32 v26, v23
	v_pk_add_f32 v[22:23], v[24:25], v[26:27]
	s_nop 0
	v_pk_add_f32 v[20:21], v[20:21], v[22:23]
	s_nop 0
	v_add_f32_e32 v1, 0, v20
	v_add_f32_e32 v1, v1, v21
	v_fmamk_f32 v1, v1, 0x3b000000, v220
	v_cmp_gt_f32_e32 vcc, s93, v1
	v_mul_f32_e32 v9, 0x4f800000, v1
	s_nop 0
	v_cndmask_b32_e32 v1, v1, v9, vcc
	v_sqrt_f32_e32 v9, v1
	s_nop 0
	v_add_u32_e32 v11, -1, v9
	v_fma_f32 v20, -v11, v9, v1
	v_cmp_ge_f32_e64 s[0:1], 0, v20
	v_add_u32_e32 v20, 1, v9
	s_nop 0
	v_cndmask_b32_e64 v11, v9, v11, s[0:1]
	v_fma_f32 v9, -v20, v9, v1
	v_cmp_lt_f32_e64 s[0:1], 0, v9
	s_nop 1
	v_cndmask_b32_e64 v9, v11, v20, s[0:1]
	v_mul_f32_e32 v11, 0x37800000, v9
	v_cndmask_b32_e32 v9, v9, v11, vcc
	v_cmp_class_f32_e32 vcc, v1, v221
	s_nop 1
	v_cndmask_b32_e32 v1, v9, v1, vcc
	v_div_scale_f32 v9, s[0:1], v1, v1, s74
	v_rcp_f32_e32 v11, v9
	s_nop 0
	v_fma_f32 v20, -v9, v11, 1.0
	v_fmac_f32_e32 v11, v20, v11
	v_div_scale_f32 v20, vcc, s74, v1, s74
	v_mul_f32_e32 v21, v20, v11
	v_fma_f32 v22, -v9, v21, v20
	v_fmac_f32_e32 v21, v22, v11
	v_fma_f32 v9, -v9, v21, v20
	v_div_fmas_f32 v9, v9, v11, v21
	v_div_fixup_f32 v20, v9, v1, s74
	v_pk_mul_f32 v[24:25], v[84:85], v[20:21] op_sel_hi:[1,0]
	v_pk_mul_f32 v[28:29], v[80:81], v[20:21] op_sel_hi:[1,0]
	v_cvt_pk_fp8_f32 v30, v24, v25
	v_cvt_pk_fp8_f32 v31, v28, v29
	v_pk_mul_f32 v[22:23], v[86:87], v[20:21] op_sel_hi:[1,0]
	v_pk_mul_f32 v[26:27], v[82:83], v[20:21] op_sel_hi:[1,0]
	v_cvt_pk_fp8_f32 v30, v22, v23 op_sel:[0,0,1]
	v_cvt_pk_fp8_f32 v31, v26, v27 op_sel:[0,0,1]
	v_pk_mul_f32 v[22:23], v[78:79], v[20:21] op_sel_hi:[1,0]
	v_pk_mul_f32 v[24:25], v[76:77], v[20:21] op_sel_hi:[1,0]
	v_pk_mul_f32 v[26:27], v[74:75], v[20:21] op_sel_hi:[1,0]
	v_pk_mul_f32 v[20:21], v[72:73], v[20:21] op_sel_hi:[1,0]
	v_mov_b32_e32 v28, v3
	v_mov_b32_e32 v29, v3
	v_cvt_pk_fp8_f32 v28, v24, v25
	v_cvt_pk_fp8_f32 v29, v20, v21
	v_mad_i64_i32 v[10:11], s[0:1], v10, s2, v[6:7]
	v_cvt_pk_fp8_f32 v28, v22, v23 op_sel:[0,0,1]
	v_cvt_pk_fp8_f32 v29, v26, v27 op_sel:[0,0,1]
	v_lshl_add_u64 v[10:11], v[10:11], 0, v[4:5]
	global_store_dwordx2 v[10:11], v[30:31], off
	v_mov_b32_e32 v30, v3
	global_store_dwordx2 v[10:11], v[28:29], off offset:128
	v_add_u32_e32 v10, 0xa0, v8
	v_ashrrev_i32_e32 v11, 31, v10
	v_lshlrev_b64 v[20:21], 6, v[10:11]
	v_lshl_add_u64 v[24:25], s[10:11], 0, v[20:21]
	s_nop 0
	v_mov_b32_e32 v31, v3
	v_add_u32_e32 v8, 0xb0, v8
	s_waitcnt vmcnt(12)
	v_mov_b32_e32 v20, v208
	v_mov_b32_e32 v21, v209
	v_mov_b32_e32 v22, v210
	v_mov_b32_e32 v23, v211
	v_mov_b32_e32 v24, v230
	v_mov_b32_e32 v25, v231
	v_mov_b32_e32 v26, v232
	v_mov_b32_e32 v27, v233
	v_mov_b32_e32 v28, v20
	v_mov_b32_e32 v29, v24
	v_mov_b32_e32 v24, v21
	v_pk_add_f32 v[20:21], v[28:29], v[24:25]
	v_mov_b32_e32 v24, v22
	v_mov_b32_e32 v25, v26
	v_mov_b32_e32 v26, v23
	v_pk_add_f32 v[22:23], v[24:25], v[26:27]
	s_nop 0
	v_pk_add_f32 v[20:21], v[20:21], v[22:23]
	s_nop 0
	v_add_f32_e32 v1, 0, v20
	v_add_f32_e32 v1, v1, v21
	v_fmamk_f32 v1, v1, 0x3b000000, v220
	v_cmp_gt_f32_e32 vcc, s93, v1
	v_mul_f32_e32 v9, 0x4f800000, v1
	s_nop 0
	v_cndmask_b32_e32 v1, v1, v9, vcc
	v_sqrt_f32_e32 v9, v1
	s_nop 0
	v_add_u32_e32 v11, -1, v9
	v_fma_f32 v20, -v11, v9, v1
	v_cmp_ge_f32_e64 s[0:1], 0, v20
	v_add_u32_e32 v20, 1, v9
	s_nop 0
	v_cndmask_b32_e64 v11, v9, v11, s[0:1]
	v_fma_f32 v9, -v20, v9, v1
	v_cmp_lt_f32_e64 s[0:1], 0, v9
	s_nop 1
	v_cndmask_b32_e64 v9, v11, v20, s[0:1]
	v_mul_f32_e32 v11, 0x37800000, v9
	v_cndmask_b32_e32 v9, v9, v11, vcc
	v_cmp_class_f32_e32 vcc, v1, v221
	s_nop 1
	v_cndmask_b32_e32 v1, v9, v1, vcc
	v_div_scale_f32 v9, s[0:1], v1, v1, s74
	v_rcp_f32_e32 v11, v9
	s_nop 0
	v_fma_f32 v20, -v9, v11, 1.0
	v_fmac_f32_e32 v11, v20, v11
	v_div_scale_f32 v20, vcc, s74, v1, s74
	v_mul_f32_e32 v21, v20, v11
	v_fma_f32 v22, -v9, v21, v20
	v_fmac_f32_e32 v21, v22, v11
	v_fma_f32 v9, -v9, v21, v20
	v_div_fmas_f32 v9, v9, v11, v21
	v_div_fixup_f32 v20, v9, v1, s74
	v_pk_mul_f32 v[24:25], v[68:69], v[20:21] op_sel_hi:[1,0]
	v_pk_mul_f32 v[28:29], v[64:65], v[20:21] op_sel_hi:[1,0]
	v_cvt_pk_fp8_f32 v30, v24, v25
	v_cvt_pk_fp8_f32 v31, v28, v29
	v_pk_mul_f32 v[22:23], v[70:71], v[20:21] op_sel_hi:[1,0]
	v_pk_mul_f32 v[26:27], v[66:67], v[20:21] op_sel_hi:[1,0]
	v_cvt_pk_fp8_f32 v30, v22, v23 op_sel:[0,0,1]
	v_cvt_pk_fp8_f32 v31, v26, v27 op_sel:[0,0,1]
	v_pk_mul_f32 v[22:23], v[62:63], v[20:21] op_sel_hi:[1,0]
	v_pk_mul_f32 v[24:25], v[60:61], v[20:21] op_sel_hi:[1,0]
	v_pk_mul_f32 v[26:27], v[58:59], v[20:21] op_sel_hi:[1,0]
	v_pk_mul_f32 v[20:21], v[56:57], v[20:21] op_sel_hi:[1,0]
	v_mov_b32_e32 v28, v3
	v_mov_b32_e32 v29, v3
	v_cvt_pk_fp8_f32 v28, v24, v25
	v_cvt_pk_fp8_f32 v29, v20, v21
	v_mad_i64_i32 v[10:11], s[0:1], v10, s2, v[6:7]
	v_cvt_pk_fp8_f32 v28, v22, v23 op_sel:[0,0,1]
	v_cvt_pk_fp8_f32 v29, v26, v27 op_sel:[0,0,1]
	v_lshl_add_u64 v[10:11], v[10:11], 0, v[4:5]
	v_ashrrev_i32_e32 v9, 31, v8
	global_store_dwordx2 v[10:11], v[30:31], off
	global_store_dwordx2 v[10:11], v[28:29], off offset:128
	v_lshlrev_b64 v[10:11], 6, v[8:9]
	v_lshl_add_u64 v[10:11], s[10:11], 0, v[10:11]
	global_load_dwordx4 v[20:23], v[10:11], off
	global_load_dwordx4 v[24:27], v[10:11], off offset:16
	s_waitcnt vmcnt(1)
	v_mov_b32_e32 v10, v20
	s_waitcnt vmcnt(0)
	v_mov_b32_e32 v11, v24
	v_mov_b32_e32 v24, v21
	v_mov_b32_e32 v20, v22
	v_mov_b32_e32 v21, v26
	v_mov_b32_e32 v26, v23
	v_pk_add_f32 v[10:11], v[10:11], v[24:25]
	v_pk_add_f32 v[20:21], v[20:21], v[26:27]
	v_mov_b32_e32 v24, v3
	v_pk_add_f32 v[10:11], v[10:11], v[20:21]
	v_mov_b32_e32 v25, v3
	v_add_f32_e32 v1, 0, v10
	v_add_f32_e32 v1, v1, v11
	v_fmamk_f32 v1, v1, 0x3b000000, v220
	v_cmp_gt_f32_e32 vcc, s93, v1
	v_mul_f32_e32 v9, 0x4f800000, v1
	s_nop 0
	v_cndmask_b32_e32 v1, v1, v9, vcc
	v_sqrt_f32_e32 v9, v1
	s_nop 0
	v_add_u32_e32 v10, -1, v9
	v_fma_f32 v11, -v10, v9, v1
	v_cmp_ge_f32_e64 s[0:1], 0, v11
	v_add_u32_e32 v11, 1, v9
	s_nop 0
	v_cndmask_b32_e64 v10, v9, v10, s[0:1]
	v_fma_f32 v9, -v11, v9, v1
	v_cmp_lt_f32_e64 s[0:1], 0, v9
	s_nop 1
	v_cndmask_b32_e64 v9, v10, v11, s[0:1]
	v_mul_f32_e32 v10, 0x37800000, v9
	v_cndmask_b32_e32 v9, v9, v10, vcc
	v_cmp_class_f32_e32 vcc, v1, v221
	v_mad_i64_i32 v[6:7], s[0:1], v8, s2, v[6:7]
	s_nop 0
	v_cndmask_b32_e32 v1, v9, v1, vcc
	v_div_scale_f32 v9, s[0:1], v1, v1, s74
	v_rcp_f32_e32 v10, v9
	v_lshl_add_u64 v[4:5], v[6:7], 0, v[4:5]
	s_mov_b64 s[0:1], -1
	v_fma_f32 v11, -v9, v10, 1.0
	v_fmac_f32_e32 v10, v11, v10
	v_div_scale_f32 v11, vcc, s74, v1, s74
	v_mul_f32_e32 v20, v11, v10
	v_fma_f32 v21, -v9, v20, v11
	v_fmac_f32_e32 v20, v21, v10
	v_fma_f32 v9, -v9, v20, v11
	v_div_fmas_f32 v9, v9, v10, v20
	v_div_fixup_f32 v10, v9, v1, s74
	v_pk_mul_f32 v[8:9], v[52:53], v[10:11] op_sel_hi:[1,0]
	v_pk_mul_f32 v[6:7], v[54:55], v[10:11] op_sel_hi:[1,0]
	v_cvt_pk_fp8_f32 v24, v8, v9
	v_pk_mul_f32 v[20:21], v[50:51], v[10:11] op_sel_hi:[1,0]
	v_pk_mul_f32 v[22:23], v[48:49], v[10:11] op_sel_hi:[1,0]
	v_pk_mul_f32 v[8:9], v[44:45], v[10:11] op_sel_hi:[1,0]
	v_cvt_pk_fp8_f32 v24, v6, v7 op_sel:[0,0,1]
	v_pk_mul_f32 v[6:7], v[46:47], v[10:11] op_sel_hi:[1,0]
	v_pk_mul_f32 v[14:15], v[14:15], v[10:11] op_sel_hi:[1,0]
	v_pk_mul_f32 v[10:11], v[12:13], v[10:11] op_sel_hi:[1,0]
	v_mov_b32_e32 v12, v3
	v_mov_b32_e32 v13, v3
	v_cvt_pk_fp8_f32 v25, v22, v23
	v_cvt_pk_fp8_f32 v12, v8, v9
	v_cvt_pk_fp8_f32 v13, v10, v11
	s_andn2_b64 vcc, exec, s[6:7]
	v_cvt_pk_fp8_f32 v25, v20, v21 op_sel:[0,0,1]
	v_cvt_pk_fp8_f32 v12, v6, v7 op_sel:[0,0,1]
	v_cvt_pk_fp8_f32 v13, v14, v15 op_sel:[0,0,1]
	global_store_dwordx2 v[4:5], v[24:25], off
	global_store_dwordx2 v[4:5], v[12:13], off offset:128
	s_cbranch_vccnz .LBB0_500
	s_andn2_b64 vcc, exec, s[4:5]
	s_cbranch_vccnz .LBB0_499
	s_barrier
	s_branch .LBB0_499

.LBB0_1943:
	v_mov_b32_e32 v4, v0
	s_lshl_b32 s0, s7, 8
	v_and_b32_e32 v5, 15, v4
	v_lshrrev_b32_e32 v4, 1, v4
	s_lshl_b32 s2, s8, 8
	s_ashr_i32 s1, s0, 31
	v_and_b32_e32 v28, 24, v4
	v_or_b32_e32 v4, s81, v5
	s_cmp_lg_u32 s55, 0
	v_mov_b32_e32 v29, v3
	v_lshlrev_b32_e32 v46, 2, v28
	v_add_u32_e32 v30, s2, v4
	s_cbranch_scc0 .LBB0_1949
	s_ashr_i32 s2, s10, 2
	s_ashr_i32 s3, s2, 31
	s_lshl_b64 s[2:3], s[2:3], 12
	s_add_u32 s31, s79, s2
	s_addc_u32 s33, s80, s3
	s_lshl_b64 s[2:3], s[0:1], 2
	s_add_u32 s2, s31, s2
	s_addc_u32 s3, s33, s3
	s_lshl_b32 s31, s24, 2
	s_add_u32 s2, s2, s31
	s_addc_u32 s3, s3, 0
	global_load_dwordx4 v[20:23], v46, s[2:3] offset:16
	global_load_dwordx4 v[24:27], v46, s[2:3]
	global_load_dwordx4 v[4:7], v46, s[2:3] offset:528
	global_load_dwordx4 v[8:11], v46, s[2:3] offset:512
	s_mov_b32 s44, 0x3e800000
	s_mov_b32 s46, 0x41800000
	v_mov_b32_e32 v42, v3
	v_mov_b32_e32 v43, v3
	v_ashrrev_i32_e32 v31, 31, v30
	v_lshlrev_b64 v[32:33], 10, v[30:31]
	v_lshl_add_u64 v[32:33], s[22:23], 0, v[32:33]
	v_lshl_add_u64 v[32:33], v[32:33], 0, s[0:1]
	v_lshl_add_u64 v[32:33], v[32:33], 0, s[24:25]
	v_lshl_add_u64 v[32:33], v[32:33], 0, v[28:29]
	v_mov_b32_e32 v44, v3
	v_mov_b32_e32 v45, v3
	s_mov_b64 s[2:3], 0x20000
	s_waitcnt vmcnt(0)
	v_pk_mul_f32 v[20:21], v[20:21], s[46:47] op_sel_hi:[1,0]
	v_pk_mul_f32 v[22:23], v[22:23], s[46:47] op_sel_hi:[1,0]
	v_pk_mul_f32 v[24:25], v[24:25], s[46:47] op_sel_hi:[1,0]
	v_pk_mul_f32 v[26:27], v[26:27], s[46:47] op_sel_hi:[1,0]
	v_pk_mul_f32 v[4:5], v[4:5], s[46:47] op_sel_hi:[1,0]
	v_pk_mul_f32 v[6:7], v[6:7], s[46:47] op_sel_hi:[1,0]
	v_pk_mul_f32 v[8:9], v[8:9], s[46:47] op_sel_hi:[1,0]
	v_pk_mul_f32 v[10:11], v[10:11], s[46:47] op_sel_hi:[1,0]
	v_pk_fma_f32 v[40:41], v[192:193], s[44:45], v[20:21] op_sel_hi:[1,0,1]
	v_pk_fma_f32 v[36:37], v[196:197], s[44:45], v[24:25] op_sel_hi:[1,0,1]
	v_cvt_pk_fp8_f32 v43, v40, v41
	v_cvt_pk_fp8_f32 v42, v36, v37
	v_pk_fma_f32 v[34:35], v[198:199], s[44:45], v[26:27] op_sel_hi:[1,0,1]
	v_pk_fma_f32 v[38:39], v[194:195], s[44:45], v[22:23] op_sel_hi:[1,0,1]
	v_cvt_pk_fp8_f32 v42, v34, v35 op_sel:[0,0,1]
	v_cvt_pk_fp8_f32 v43, v38, v39 op_sel:[0,0,1]
	v_pk_fma_f32 v[36:37], v[164:165], s[44:45], v[8:9] op_sel_hi:[1,0,1]
	v_pk_fma_f32 v[40:41], v[160:161], s[44:45], v[4:5] op_sel_hi:[1,0,1]
	global_store_dwordx2 v[32:33], v[42:43], off
	v_mov_b32_e32 v42, v3
	v_mov_b32_e32 v43, v3
	v_cvt_pk_fp8_f32 v42, v36, v37
	v_cvt_pk_fp8_f32 v43, v40, v41
	v_pk_fma_f32 v[34:35], v[166:167], s[44:45], v[10:11] op_sel_hi:[1,0,1]
	v_pk_fma_f32 v[38:39], v[162:163], s[44:45], v[6:7] op_sel_hi:[1,0,1]
	v_cvt_pk_fp8_f32 v42, v34, v35 op_sel:[0,0,1]
	v_cvt_pk_fp8_f32 v43, v38, v39 op_sel:[0,0,1]
	v_pk_fma_f32 v[38:39], v[188:189], s[44:45], v[24:25] op_sel_hi:[1,0,1]
	v_or_b32_e32 v34, 16, v30
	global_store_dwordx2 v[32:33], v[42:43], off offset:128
	v_pk_fma_f32 v[42:43], v[184:185], s[44:45], v[20:21] op_sel_hi:[1,0,1]
	v_cvt_pk_fp8_f32 v44, v38, v39
	v_ashrrev_i32_e32 v35, 31, v34
	v_cvt_pk_fp8_f32 v45, v42, v43
	v_pk_fma_f32 v[36:37], v[190:191], s[44:45], v[26:27] op_sel_hi:[1,0,1]
	v_pk_fma_f32 v[40:41], v[186:187], s[44:45], v[22:23] op_sel_hi:[1,0,1]
	v_lshlrev_b64 v[34:35], 10, v[34:35]
	v_lshl_add_u64 v[34:35], s[22:23], 0, v[34:35]
	v_cvt_pk_fp8_f32 v44, v36, v37 op_sel:[0,0,1]
	v_cvt_pk_fp8_f32 v45, v40, v41 op_sel:[0,0,1]
	v_lshl_add_u64 v[34:35], v[34:35], 0, s[0:1]
	v_lshl_add_u64 v[34:35], v[34:35], 0, s[24:25]
	v_lshl_add_u64 v[34:35], v[34:35], 0, v[28:29]
	v_pk_fma_f32 v[38:39], v[156:157], s[44:45], v[8:9] op_sel_hi:[1,0,1]
	v_pk_fma_f32 v[42:43], v[152:153], s[44:45], v[4:5] op_sel_hi:[1,0,1]
	global_store_dwordx2 v[34:35], v[44:45], off
	v_mov_b32_e32 v44, v3
	v_mov_b32_e32 v45, v3
	v_cvt_pk_fp8_f32 v44, v38, v39
	v_cvt_pk_fp8_f32 v45, v42, v43
	v_pk_fma_f32 v[36:37], v[158:159], s[44:45], v[10:11] op_sel_hi:[1,0,1]
	v_pk_fma_f32 v[40:41], v[154:155], s[44:45], v[6:7] op_sel_hi:[1,0,1]
	v_cvt_pk_fp8_f32 v44, v36, v37 op_sel:[0,0,1]
	v_cvt_pk_fp8_f32 v45, v40, v41 op_sel:[0,0,1]
	v_pk_fma_f32 v[38:39], v[180:181], s[44:45], v[24:25] op_sel_hi:[1,0,1]
	v_pk_fma_f32 v[36:37], v[182:183], s[44:45], v[26:27] op_sel_hi:[1,0,1]
	v_mov_b64_e32 v[42:43], v[38:39]
	v_pk_fma_f32 v[38:39], v[176:177], s[44:45], v[20:21] op_sel_hi:[1,0,1]
	global_store_dwordx2 v[34:35], v[44:45], off offset:128
	v_mov_b32_e32 v44, v3
	v_mov_b32_e32 v45, v3
	v_cvt_pk_fp8_f32 v44, v42, v43
	v_cvt_pk_fp8_f32 v45, v38, v39
	v_or_b32_e32 v34, 32, v30
	v_ashrrev_i32_e32 v35, 31, v34
	v_mov_b64_e32 v[40:41], v[36:37]
	v_pk_fma_f32 v[36:37], v[178:179], s[44:45], v[22:23] op_sel_hi:[1,0,1]
	v_lshlrev_b64 v[34:35], 10, v[34:35]
	v_lshl_add_u64 v[34:35], s[22:23], 0, v[34:35]
	v_cvt_pk_fp8_f32 v44, v40, v41 op_sel:[0,0,1]
	v_cvt_pk_fp8_f32 v45, v36, v37 op_sel:[0,0,1]
	v_lshl_add_u64 v[34:35], v[34:35], 0, s[0:1]
	v_lshl_add_u64 v[34:35], v[34:35], 0, s[24:25]
	v_lshl_add_u64 v[34:35], v[34:35], 0, v[28:29]
	v_pk_fma_f32 v[38:39], v[148:149], s[44:45], v[8:9] op_sel_hi:[1,0,1]
	v_pk_fma_f32 v[42:43], v[144:145], s[44:45], v[4:5] op_sel_hi:[1,0,1]
	global_store_dwordx2 v[34:35], v[44:45], off
	v_mov_b32_e32 v44, v3
	v_mov_b32_e32 v45, v3
	v_cvt_pk_fp8_f32 v44, v38, v39
	v_cvt_pk_fp8_f32 v45, v42, v43
	v_pk_fma_f32 v[36:37], v[150:151], s[44:45], v[10:11] op_sel_hi:[1,0,1]
	v_pk_fma_f32 v[40:41], v[146:147], s[44:45], v[6:7] op_sel_hi:[1,0,1]
	v_cvt_pk_fp8_f32 v44, v36, v37 op_sel:[0,0,1]
	v_cvt_pk_fp8_f32 v45, v40, v41 op_sel:[0,0,1]
	v_pk_fma_f32 v[38:39], v[172:173], s[44:45], v[24:25] op_sel_hi:[1,0,1]
	v_pk_fma_f32 v[42:43], v[168:169], s[44:45], v[20:21] op_sel_hi:[1,0,1]
	global_store_dwordx2 v[34:35], v[44:45], off offset:128
	v_mov_b32_e32 v44, v3
	v_mov_b32_e32 v45, v3
	v_cvt_pk_fp8_f32 v44, v38, v39
	v_cvt_pk_fp8_f32 v45, v42, v43
	v_or_b32_e32 v34, 48, v30
	v_ashrrev_i32_e32 v35, 31, v34
	v_pk_fma_f32 v[36:37], v[174:175], s[44:45], v[26:27] op_sel_hi:[1,0,1]
	v_pk_fma_f32 v[40:41], v[170:171], s[44:45], v[22:23] op_sel_hi:[1,0,1]
	v_lshlrev_b64 v[34:35], 10, v[34:35]
	v_lshl_add_u64 v[34:35], s[22:23], 0, v[34:35]
	v_cvt_pk_fp8_f32 v44, v36, v37 op_sel:[0,0,1]
	v_cvt_pk_fp8_f32 v45, v40, v41 op_sel:[0,0,1]
	v_lshl_add_u64 v[34:35], v[34:35], 0, s[0:1]
	v_lshl_add_u64 v[34:35], v[34:35], 0, s[24:25]
	v_lshl_add_u64 v[34:35], v[34:35], 0, v[28:29]
	v_pk_fma_f32 v[38:39], v[140:141], s[44:45], v[8:9] op_sel_hi:[1,0,1]
	v_pk_fma_f32 v[42:43], v[136:137], s[44:45], v[4:5] op_sel_hi:[1,0,1]
	global_store_dwordx2 v[34:35], v[44:45], off
	v_mov_b32_e32 v44, v3
	v_mov_b32_e32 v45, v3
	v_cvt_pk_fp8_f32 v44, v38, v39
	v_cvt_pk_fp8_f32 v45, v42, v43
	v_pk_fma_f32 v[36:37], v[142:143], s[44:45], v[10:11] op_sel_hi:[1,0,1]
	v_pk_fma_f32 v[40:41], v[138:139], s[44:45], v[6:7] op_sel_hi:[1,0,1]
	v_cvt_pk_fp8_f32 v44, v36, v37 op_sel:[0,0,1]
	v_cvt_pk_fp8_f32 v45, v40, v41 op_sel:[0,0,1]
	v_pk_fma_f32 v[38:39], v[132:133], s[44:45], v[24:25] op_sel_hi:[1,0,1]
	v_pk_fma_f32 v[42:43], v[128:129], s[44:45], v[20:21] op_sel_hi:[1,0,1]
	global_store_dwordx2 v[34:35], v[44:45], off offset:128
	v_mov_b32_e32 v44, v3
	v_mov_b32_e32 v45, v3
	v_cvt_pk_fp8_f32 v44, v38, v39
	v_cvt_pk_fp8_f32 v45, v42, v43
	v_pk_fma_f32 v[36:37], v[134:135], s[44:45], v[26:27] op_sel_hi:[1,0,1]
	v_pk_fma_f32 v[40:41], v[130:131], s[44:45], v[22:23] op_sel_hi:[1,0,1]
	v_cvt_pk_fp8_f32 v44, v36, v37 op_sel:[0,0,1]
	v_cvt_pk_fp8_f32 v45, v40, v41 op_sel:[0,0,1]
	v_lshl_add_u64 v[34:35], v[32:33], 0, s[2:3]
	s_mov_b32 s2, 0x20000
	v_add_co_u32_e32 v36, vcc, s2, v32
	v_pk_fma_f32 v[38:39], v[100:101], s[44:45], v[8:9] op_sel_hi:[1,0,1]
	s_nop 0
	v_addc_co_u32_e32 v37, vcc, 0, v33, vcc
	v_pk_fma_f32 v[42:43], v[96:97], s[44:45], v[4:5] op_sel_hi:[1,0,1]
	global_store_dwordx2 v[36:37], v[44:45], off
	v_mov_b32_e32 v44, v3
	v_mov_b32_e32 v45, v3
	v_cvt_pk_fp8_f32 v44, v38, v39
	v_cvt_pk_fp8_f32 v45, v42, v43
	v_pk_fma_f32 v[36:37], v[102:103], s[44:45], v[10:11] op_sel_hi:[1,0,1]
	v_pk_fma_f32 v[40:41], v[98:99], s[44:45], v[6:7] op_sel_hi:[1,0,1]
	v_cvt_pk_fp8_f32 v44, v36, v37 op_sel:[0,0,1]
	v_cvt_pk_fp8_f32 v45, v40, v41 op_sel:[0,0,1]
	v_pk_fma_f32 v[38:39], v[124:125], s[44:45], v[24:25] op_sel_hi:[1,0,1]
	v_pk_fma_f32 v[42:43], v[120:121], s[44:45], v[20:21] op_sel_hi:[1,0,1]
	global_store_dwordx2 v[34:35], v[44:45], off offset:128
	v_mov_b32_e32 v44, v3
	v_mov_b32_e32 v45, v3
	v_cvt_pk_fp8_f32 v44, v38, v39
	v_cvt_pk_fp8_f32 v45, v42, v43
	v_pk_fma_f32 v[36:37], v[126:127], s[44:45], v[26:27] op_sel_hi:[1,0,1]
	v_pk_fma_f32 v[40:41], v[122:123], s[44:45], v[22:23] op_sel_hi:[1,0,1]
	s_mov_b64 s[2:3], 0x24000
	v_cvt_pk_fp8_f32 v44, v36, v37 op_sel:[0,0,1]
	v_cvt_pk_fp8_f32 v45, v40, v41 op_sel:[0,0,1]
	v_lshl_add_u64 v[34:35], v[32:33], 0, s[2:3]
	s_mov_b32 s2, 0x24000
	v_add_co_u32_e32 v36, vcc, s2, v32
	v_pk_fma_f32 v[38:39], v[92:93], s[44:45], v[8:9] op_sel_hi:[1,0,1]
	s_nop 0
	v_addc_co_u32_e32 v37, vcc, 0, v33, vcc
	v_pk_fma_f32 v[42:43], v[88:89], s[44:45], v[4:5] op_sel_hi:[1,0,1]
	global_store_dwordx2 v[36:37], v[44:45], off
	v_mov_b32_e32 v44, v3
	v_mov_b32_e32 v45, v3
	v_cvt_pk_fp8_f32 v44, v38, v39
	v_cvt_pk_fp8_f32 v45, v42, v43
	v_pk_fma_f32 v[36:37], v[94:95], s[44:45], v[10:11] op_sel_hi:[1,0,1]
	v_pk_fma_f32 v[40:41], v[90:91], s[44:45], v[6:7] op_sel_hi:[1,0,1]
	v_cvt_pk_fp8_f32 v44, v36, v37 op_sel:[0,0,1]
	v_cvt_pk_fp8_f32 v45, v40, v41 op_sel:[0,0,1]
	v_pk_fma_f32 v[38:39], v[116:117], s[44:45], v[24:25] op_sel_hi:[1,0,1]
	v_pk_fma_f32 v[42:43], v[112:113], s[44:45], v[20:21] op_sel_hi:[1,0,1]
	global_store_dwordx2 v[34:35], v[44:45], off offset:128
	v_mov_b32_e32 v44, v3
	v_mov_b32_e32 v45, v3
	v_cvt_pk_fp8_f32 v44, v38, v39
	v_cvt_pk_fp8_f32 v45, v42, v43
	v_pk_fma_f32 v[36:37], v[118:119], s[44:45], v[26:27] op_sel_hi:[1,0,1]
	v_pk_fma_f32 v[40:41], v[114:115], s[44:45], v[22:23] op_sel_hi:[1,0,1]
	s_mov_b64 s[2:3], 0x28000
	v_cvt_pk_fp8_f32 v44, v36, v37 op_sel:[0,0,1]
	v_cvt_pk_fp8_f32 v45, v40, v41 op_sel:[0,0,1]
	v_lshl_add_u64 v[34:35], v[32:33], 0, s[2:3]
	s_mov_b32 s2, 0x28000
	v_add_co_u32_e32 v36, vcc, s2, v32
	v_pk_fma_f32 v[38:39], v[84:85], s[44:45], v[8:9] op_sel_hi:[1,0,1]
	s_nop 0
	v_addc_co_u32_e32 v37, vcc, 0, v33, vcc
	global_store_dwordx2 v[36:37], v[44:45], off
	v_mov_b32_e32 v44, v3
	v_pk_fma_f32 v[42:43], v[80:81], s[44:45], v[4:5] op_sel_hi:[1,0,1]
	v_cvt_pk_fp8_f32 v44, v38, v39
	v_mov_b32_e32 v45, v3
	v_pk_fma_f32 v[36:37], v[86:87], s[44:45], v[10:11] op_sel_hi:[1,0,1]
	v_cvt_pk_fp8_f32 v45, v42, v43
	v_pk_fma_f32 v[24:25], v[108:109], s[44:45], v[24:25] op_sel_hi:[1,0,1]
	v_pk_fma_f32 v[20:21], v[104:105], s[44:45], v[20:21] op_sel_hi:[1,0,1]
	v_pk_fma_f32 v[40:41], v[82:83], s[44:45], v[6:7] op_sel_hi:[1,0,1]
	v_cvt_pk_fp8_f32 v44, v36, v37 op_sel:[0,0,1]
	v_mov_b32_e32 v36, v3
	v_mov_b32_e32 v37, v3
	v_cvt_pk_fp8_f32 v36, v24, v25
	v_cvt_pk_fp8_f32 v37, v20, v21
	v_cvt_pk_fp8_f32 v45, v40, v41 op_sel:[0,0,1]
	v_pk_fma_f32 v[26:27], v[110:111], s[44:45], v[26:27] op_sel_hi:[1,0,1]
	v_pk_fma_f32 v[22:23], v[106:107], s[44:45], v[22:23] op_sel_hi:[1,0,1]
	s_mov_b64 s[2:3], 0x2c000
	v_cvt_pk_fp8_f32 v36, v26, v27 op_sel:[0,0,1]
	v_cvt_pk_fp8_f32 v37, v22, v23 op_sel:[0,0,1]
	global_store_dwordx2 v[34:35], v[44:45], off offset:128
	v_lshl_add_u64 v[34:35], v[32:33], 0, s[2:3]
	s_mov_b32 s2, 0x2c000
	v_add_co_u32_e32 v20, vcc, s2, v32
	v_pk_fma_f32 v[8:9], v[76:77], s[44:45], v[8:9] op_sel_hi:[1,0,1]
	s_nop 0
	v_addc_co_u32_e32 v21, vcc, 0, v33, vcc
	v_pk_fma_f32 v[4:5], v[12:13], s[44:45], v[4:5] op_sel_hi:[1,0,1]
	global_store_dwordx2 v[20:21], v[36:37], off
	v_mov_b32_e32 v20, v3
	v_mov_b32_e32 v21, v3
	v_cvt_pk_fp8_f32 v20, v8, v9
	v_cvt_pk_fp8_f32 v21, v4, v5
	v_pk_fma_f32 v[10:11], v[78:79], s[44:45], v[10:11] op_sel_hi:[1,0,1]
	v_pk_fma_f32 v[6:7], v[14:15], s[44:45], v[6:7] op_sel_hi:[1,0,1]
	v_cvt_pk_fp8_f32 v20, v10, v11 op_sel:[0,0,1]
	v_cvt_pk_fp8_f32 v21, v6, v7 op_sel:[0,0,1]
	global_store_dwordx2 v[34:35], v[20:21], off offset:128
	s_cbranch_execnz .LBB0_1946
